# baseline (speedup 1.0000x reference)
_ZN12_GLOBAL__N_112oproj_kernelEPKDF16_S1_PKfPf:
	s_load_dwordx8 s[4:11], s[0:1], 0x0
	s_lshl_b32 s1, s2, 4
	s_and_b32 s3, s1, 0x180
	s_lshr_b32 s1, s2, 2
	s_and_b32 s0, s2, 7
	s_and_b32 s1, s1, 0x1fffff8
	s_or_b32 s0, s1, s0
	s_lshl_b32 s0, s0, 7
	s_mov_b32 s1, 0
	s_lshl_b64 s[12:13], s[0:1], 10
	v_lshrrev_b32_e32 v36, 3, v0
	v_and_b32_e32 v250, 0x5f, v0
	v_or_b32_e32 v250, s3, v250
	v_lshlrev_b32_e32 v250, 2, v250
	v_lshlrev_b32_e32 v238, 10, v36
	v_mov_b32_e32 v239, 0
	v_lshlrev_b32_e32 v37, 4, v0
	s_waitcnt lgkmcnt(0)
	s_add_u32 s4, s4, s12
	s_addc_u32 s5, s5, s13
	global_load_dword v251, v250, s[8:9]
	global_load_dword v252, v250, s[8:9] offset:128
	v_lshl_add_u64 v[2:3], s[4:5], 0, v[238:239]
	v_and_b32_e32 v238, 0x70, v37
	v_lshl_add_u64 v[66:67], v[2:3], 0, v[238:239]
	s_mov_b32 s1, 0x8000
	v_add_co_u32_e32 v68, vcc, s1, v66
	s_mov_b32 s2, 0x10000
	s_nop 0
	v_addc_co_u32_e32 v69, vcc, 0, v67, vcc
	v_add_co_u32_e32 v70, vcc, s2, v66
	v_or_b32_e32 v1, s3, v36
	s_nop 0
	v_addc_co_u32_e32 v71, vcc, 0, v67, vcc
	s_mov_b32 s4, 0x18000
	v_add_co_u32_e32 v72, vcc, s4, v66
	v_lshl_add_u64 v[18:19], s[6:7], 0, v[238:239]
	v_lshlrev_b32_e32 v34, 10, v1
	v_mov_b32_e32 v35, v239
	v_addc_co_u32_e32 v73, vcc, 0, v67, vcc
	v_lshl_add_u64 v[74:75], v[18:19], 0, v[34:35]
	v_add_co_u32_e32 v76, vcc, s1, v74
	global_load_dwordx4 v[2:5], v[66:67], off
	global_load_dwordx4 v[6:9], v[68:69], off
	v_addc_co_u32_e32 v77, vcc, 0, v75, vcc
	v_add_co_u32_e32 v78, vcc, s2, v74
	global_load_dwordx4 v[10:13], v[70:71], off
	global_load_dwordx4 v[14:17], v[72:73], off
	v_addc_co_u32_e32 v79, vcc, 0, v75, vcc
	v_add_co_u32_e32 v80, vcc, s4, v74
	global_load_dwordx4 v[18:21], v[74:75], off
	global_load_dwordx4 v[22:25], v[76:77], off
	v_addc_co_u32_e32 v81, vcc, 0, v75, vcc
	global_load_dwordx4 v[26:29], v[78:79], off
	global_load_dwordx4 v[30:33], v[80:81], off
	v_lshl_add_u64 v[34:35], s[6:7], 0, v[34:35]
	s_movk_i32 s5, 0x70
	v_xor_b32_e32 v37, v37, v0
	v_lshlrev_b32_e32 v36, 7, v36
	v_lshl_add_u64 v[34:35], v[34:35], 0, v[238:239]
	v_and_or_b32 v82, v37, s5, v36
	v_add_co_u32_e32 v36, vcc, s1, v34
	global_load_dwordx4 v[100:103], v[66:67], off offset:128
	global_load_dwordx4 v[104:107], v[68:69], off offset:128
	global_load_dwordx4 v[112:115], v[70:71], off offset:128
	global_load_dwordx4 v[116:119], v[72:73], off offset:128
	v_addc_co_u32_e32 v37, vcc, 0, v35, vcc
	global_load_dwordx4 v[120:123], v[34:35], off offset:128
	global_load_dwordx4 v[124:127], v[36:37], off offset:128
	v_add_co_u32_e32 v36, vcc, s2, v34
	v_lshrrev_b32_e32 v1, 1, v0
	s_nop 0
	v_addc_co_u32_e32 v37, vcc, 0, v35, vcc
	v_add_co_u32_e32 v34, vcc, s4, v34
	v_lshrrev_b32_e32 v38, 5, v0
	s_nop 0
	v_addc_co_u32_e32 v35, vcc, 0, v35, vcc
	global_load_dwordx4 v[128:131], v[36:37], off offset:128
	global_load_dwordx4 v[132:135], v[34:35], off offset:128
	v_and_b32_e32 v1, 64, v1
	v_bfe_u32 v144, v0, 1, 3
	v_and_or_b32 v39, v0, 31, v1
	v_lshlrev_b32_e32 v87, 7, v39
	v_bfe_u32 v240, v0, 5, 1
	v_bitop3_b32 v85, v240, v144, 2 bitop3:0x36
	v_lshlrev_b32_e32 v86, 4, v85
	v_or_b32_e32 v85, v87, v86
	v_mov_b32_e32 v241, v239
	s_waitcnt vmcnt(15)
	ds_write_b128 v82, v[2:5]
	s_waitcnt vmcnt(14)
	ds_write_b128 v82, v[6:9] offset:4096
	s_waitcnt vmcnt(13)
	ds_write_b128 v82, v[10:13] offset:8192
	s_waitcnt vmcnt(12)
	ds_write_b128 v82, v[14:17] offset:12288
	s_waitcnt vmcnt(11)
	ds_write_b128 v82, v[18:21] offset:16384
	s_waitcnt vmcnt(10)
	ds_write_b128 v82, v[22:25] offset:20480
	s_waitcnt vmcnt(9)
	ds_write_b128 v82, v[26:29] offset:24576
	s_waitcnt vmcnt(8)
	ds_write_b128 v82, v[30:33] offset:28672
	v_bitop3_b32 v2, v38, v144, 1 bitop3:0x6c
	v_lshlrev_b32_e32 v6, 4, v2
	v_or_b32_e32 v83, v87, v6
	s_waitcnt lgkmcnt(0)
	s_barrier
	ds_read_b128 v[2:5], v83
	v_lshlrev_b32_e32 v7, 7, v0
	v_and_b32_e32 v145, 0x2f80, v7
	v_or_b32_e32 v84, v145, v6
	ds_read_b128 v[6:9], v84 offset:16384
	ds_read_b128 v[10:13], v83 offset:4096
	ds_read_b128 v[14:17], v84 offset:20480
	ds_read_b128 v[88:91], v85
	s_waitcnt lgkmcnt(3)
	v_mfma_f32_32x32x16_f16 v[50:65], v[2:5], v[6:9], 0
	v_or_b32_e32 v86, v145, v86
	ds_read_b128 v[92:95], v86 offset:16384
	ds_read_b128 v[96:99], v85 offset:4096
	ds_read_b128 v[108:111], v86 offset:20480
	v_and_b32_e32 v0, 0x5f, v0
	v_or_b32_e32 v0, s3, v0
	v_lshlrev_b32_e32 v238, 2, v0
	v_lshlrev_b32_e32 v0, 2, v240
	s_waitcnt lgkmcnt(4)
	v_mfma_f32_32x32x16_f16 v[18:33], v[2:5], v[14:17], 0
	v_mfma_f32_32x32x16_f16 v[34:49], v[10:13], v[6:9], 0
	v_mfma_f32_32x32x16_f16 v[2:17], v[10:13], v[14:17], 0
	s_waitcnt lgkmcnt(2)
	v_mfma_f32_32x32x16_f16 v[50:65], v[88:91], v[92:95], v[50:65]
	s_waitcnt lgkmcnt(0)
	v_mfma_f32_32x32x16_f16 v[18:33], v[88:91], v[108:111], v[18:33]
	v_bitop3_b32 v88, v240, v144, 4 bitop3:0x36
	v_lshlrev_b32_e32 v88, 4, v88
	v_or_b32_e32 v90, v87, v88
	v_mfma_f32_32x32x16_f16 v[34:49], v[96:99], v[92:95], v[34:49]
	v_or_b32_e32 v94, v145, v88
	v_bitop3_b32 v88, v240, v144, 6 bitop3:0x36
	v_lshlrev_b32_e32 v88, 4, v88
	v_or3_b32 v240, s0, v1, v0
	v_lshl_add_u64 v[0:1], s[10:11], 0, v[238:239]
	v_mfma_f32_32x32x16_f16 v[2:17], v[96:99], v[108:111], v[2:17]
	ds_read_b128 v[96:99], v90
	ds_read_b128 v[108:111], v94 offset:16384
	ds_read_b128 v[136:139], v90 offset:4096
	ds_read_b128 v[140:143], v94 offset:20480
	s_waitcnt lgkmcnt(2)
	v_mfma_f32_32x32x16_f16 v[50:65], v[96:99], v[108:111], v[50:65]
	s_waitcnt lgkmcnt(0)
	v_mfma_f32_32x32x16_f16 v[18:33], v[96:99], v[140:143], v[18:33]
	v_or_b32_e32 v98, v87, v88
	v_mfma_f32_32x32x16_f16 v[34:49], v[136:139], v[108:111], v[34:49]
	v_or_b32_e32 v110, v145, v88
	v_mfma_f32_32x32x16_f16 v[2:17], v[136:139], v[140:143], v[2:17]
	ds_read_b128 v[136:139], v98
	ds_read_b128 v[140:143], v110 offset:16384
	ds_read_b128 v[144:147], v98 offset:4096
	ds_read_b128 v[148:151], v110 offset:20480
	s_waitcnt lgkmcnt(2)
	v_mfma_f32_32x32x16_f16 v[50:65], v[136:139], v[140:143], v[50:65]
	s_waitcnt lgkmcnt(0)
	v_mfma_f32_32x32x16_f16 v[18:33], v[136:139], v[148:151], v[18:33]
	v_mfma_f32_32x32x16_f16 v[34:49], v[144:147], v[140:143], v[34:49]
	global_load_dwordx4 v[136:139], v[66:67], off offset:256
	global_load_dwordx4 v[140:143], v[68:69], off offset:256
	global_load_dwordx4 v[152:155], v[70:71], off offset:256
	global_load_dwordx4 v[156:159], v[72:73], off offset:256
	global_load_dwordx4 v[160:163], v[74:75], off offset:256
	global_load_dwordx4 v[164:167], v[76:77], off offset:256
	global_load_dwordx4 v[168:171], v[78:79], off offset:256
	global_load_dwordx4 v[172:175], v[80:81], off offset:256
	s_waitcnt vmcnt(15)
	ds_write_b128 v82, v[100:103] offset:32768
	s_waitcnt vmcnt(14)
	ds_write_b128 v82, v[104:107] offset:36864
	s_waitcnt vmcnt(13)
	ds_write_b128 v82, v[112:115] offset:40960
	s_waitcnt vmcnt(12)
	ds_write_b128 v82, v[116:119] offset:45056
	s_waitcnt vmcnt(11)
	ds_write_b128 v82, v[120:123] offset:49152
	s_waitcnt vmcnt(10)
	ds_write_b128 v82, v[124:127] offset:53248
	s_waitcnt vmcnt(9)
	ds_write_b128 v82, v[128:131] offset:57344
	s_waitcnt vmcnt(8)
	ds_write_b128 v82, v[132:135] offset:61440
	s_waitcnt lgkmcnt(0)
	s_barrier
	ds_read_b128 v[100:103], v83 offset:32768
	ds_read_b128 v[104:107], v84 offset:49152
	ds_read_b128 v[112:115], v83 offset:36864
	ds_read_b128 v[116:119], v84 offset:53248
	v_mfma_f32_32x32x16_f16 v[2:17], v[144:147], v[148:151], v[2:17]
	s_waitcnt lgkmcnt(2)
	v_mfma_f32_32x32x16_f16 v[50:65], v[100:103], v[104:107], v[50:65]
	s_waitcnt lgkmcnt(0)
	v_mfma_f32_32x32x16_f16 v[18:33], v[100:103], v[116:119], v[18:33]
	v_mfma_f32_32x32x16_f16 v[34:49], v[112:115], v[104:107], v[34:49]
	v_mfma_f32_32x32x16_f16 v[2:17], v[112:115], v[116:119], v[2:17]
	ds_read_b128 v[100:103], v85 offset:32768
	ds_read_b128 v[104:107], v86 offset:49152
	ds_read_b128 v[112:115], v85 offset:36864
	ds_read_b128 v[116:119], v86 offset:53248
	s_waitcnt lgkmcnt(2)
	v_mfma_f32_32x32x16_f16 v[50:65], v[100:103], v[104:107], v[50:65]
	s_waitcnt lgkmcnt(0)
	v_mfma_f32_32x32x16_f16 v[18:33], v[100:103], v[116:119], v[18:33]
	v_mfma_f32_32x32x16_f16 v[34:49], v[112:115], v[104:107], v[34:49]
	v_mfma_f32_32x32x16_f16 v[2:17], v[112:115], v[116:119], v[2:17]
	ds_read_b128 v[100:103], v90 offset:32768
	ds_read_b128 v[104:107], v94 offset:49152
	ds_read_b128 v[112:115], v90 offset:36864
	ds_read_b128 v[116:119], v94 offset:53248
	s_waitcnt lgkmcnt(2)
	v_mfma_f32_32x32x16_f16 v[50:65], v[100:103], v[104:107], v[50:65]
	s_waitcnt lgkmcnt(0)
	v_mfma_f32_32x32x16_f16 v[18:33], v[100:103], v[116:119], v[18:33]
	v_mfma_f32_32x32x16_f16 v[34:49], v[112:115], v[104:107], v[34:49]
	v_mfma_f32_32x32x16_f16 v[2:17], v[112:115], v[116:119], v[2:17]
	ds_read_b128 v[100:103], v98 offset:32768
	ds_read_b128 v[104:107], v110 offset:49152
	ds_read_b128 v[112:115], v98 offset:36864
	ds_read_b128 v[116:119], v110 offset:53248
	s_waitcnt lgkmcnt(2)
	v_mfma_f32_32x32x16_f16 v[50:65], v[100:103], v[104:107], v[50:65]
	s_waitcnt lgkmcnt(0)
	v_mfma_f32_32x32x16_f16 v[18:33], v[100:103], v[116:119], v[18:33]
	v_mfma_f32_32x32x16_f16 v[34:49], v[112:115], v[104:107], v[34:49]
	global_load_dwordx4 v[100:103], v[66:67], off offset:384
	global_load_dwordx4 v[104:107], v[68:69], off offset:384
	global_load_dwordx4 v[120:123], v[70:71], off offset:384
	global_load_dwordx4 v[124:127], v[72:73], off offset:384
	global_load_dwordx4 v[128:131], v[74:75], off offset:384
	global_load_dwordx4 v[132:135], v[76:77], off offset:384
	global_load_dwordx4 v[144:147], v[78:79], off offset:384
	global_load_dwordx4 v[148:151], v[80:81], off offset:384
	s_waitcnt vmcnt(15)
	ds_write_b128 v82, v[136:139]
	s_waitcnt vmcnt(14)
	ds_write_b128 v82, v[140:143] offset:4096
	s_waitcnt vmcnt(13)
	ds_write_b128 v82, v[152:155] offset:8192
	s_waitcnt vmcnt(12)
	ds_write_b128 v82, v[156:159] offset:12288
	s_waitcnt vmcnt(11)
	ds_write_b128 v82, v[160:163] offset:16384
	s_waitcnt vmcnt(10)
	ds_write_b128 v82, v[164:167] offset:20480
	s_waitcnt vmcnt(9)
	ds_write_b128 v82, v[168:171] offset:24576
	s_waitcnt vmcnt(8)
	ds_write_b128 v82, v[172:175] offset:28672
	s_waitcnt lgkmcnt(0)
	s_barrier
	v_mfma_f32_32x32x16_f16 v[2:17], v[112:115], v[116:119], v[2:17]
	ds_read_b128 v[112:115], v83
	ds_read_b128 v[116:119], v84 offset:16384
	ds_read_b128 v[136:139], v83 offset:4096
	ds_read_b128 v[140:143], v84 offset:20480
	s_waitcnt lgkmcnt(2)
	v_mfma_f32_32x32x16_f16 v[50:65], v[112:115], v[116:119], v[50:65]
	s_waitcnt lgkmcnt(0)
	v_mfma_f32_32x32x16_f16 v[18:33], v[112:115], v[140:143], v[18:33]
	v_mfma_f32_32x32x16_f16 v[34:49], v[136:139], v[116:119], v[34:49]
	v_mfma_f32_32x32x16_f16 v[2:17], v[136:139], v[140:143], v[2:17]
	ds_read_b128 v[112:115], v85
	ds_read_b128 v[116:119], v86 offset:16384
	ds_read_b128 v[136:139], v85 offset:4096
	ds_read_b128 v[140:143], v86 offset:20480
	s_waitcnt lgkmcnt(2)
	v_mfma_f32_32x32x16_f16 v[50:65], v[112:115], v[116:119], v[50:65]
	s_waitcnt lgkmcnt(0)
	v_mfma_f32_32x32x16_f16 v[18:33], v[112:115], v[140:143], v[18:33]
	v_mfma_f32_32x32x16_f16 v[34:49], v[136:139], v[116:119], v[34:49]
	v_mfma_f32_32x32x16_f16 v[2:17], v[136:139], v[140:143], v[2:17]
	ds_read_b128 v[112:115], v90
	ds_read_b128 v[116:119], v94 offset:16384
	ds_read_b128 v[136:139], v90 offset:4096
	ds_read_b128 v[140:143], v94 offset:20480
	s_waitcnt lgkmcnt(2)
	v_mfma_f32_32x32x16_f16 v[50:65], v[112:115], v[116:119], v[50:65]
	s_waitcnt lgkmcnt(0)
	v_mfma_f32_32x32x16_f16 v[18:33], v[112:115], v[140:143], v[18:33]
	v_mfma_f32_32x32x16_f16 v[34:49], v[136:139], v[116:119], v[34:49]
	v_mfma_f32_32x32x16_f16 v[2:17], v[136:139], v[140:143], v[2:17]
	ds_read_b128 v[112:115], v98
	ds_read_b128 v[116:119], v110 offset:16384
	ds_read_b128 v[136:139], v98 offset:4096
	ds_read_b128 v[140:143], v110 offset:20480
	s_waitcnt lgkmcnt(2)
	v_mfma_f32_32x32x16_f16 v[50:65], v[112:115], v[116:119], v[50:65]
	s_waitcnt lgkmcnt(0)
	v_mfma_f32_32x32x16_f16 v[18:33], v[112:115], v[140:143], v[18:33]
	v_mfma_f32_32x32x16_f16 v[34:49], v[136:139], v[116:119], v[34:49]
	global_load_dwordx4 v[112:115], v[66:67], off offset:512
	global_load_dwordx4 v[116:119], v[68:69], off offset:512
	global_load_dwordx4 v[152:155], v[70:71], off offset:512
	global_load_dwordx4 v[156:159], v[72:73], off offset:512
	global_load_dwordx4 v[160:163], v[74:75], off offset:512
	global_load_dwordx4 v[164:167], v[76:77], off offset:512
	global_load_dwordx4 v[168:171], v[78:79], off offset:512
	global_load_dwordx4 v[172:175], v[80:81], off offset:512
	s_waitcnt vmcnt(15)
	ds_write_b128 v82, v[100:103] offset:32768
	s_waitcnt vmcnt(14)
	ds_write_b128 v82, v[104:107] offset:36864
	s_waitcnt vmcnt(13)
	ds_write_b128 v82, v[120:123] offset:40960
	s_waitcnt vmcnt(12)
	ds_write_b128 v82, v[124:127] offset:45056
	s_waitcnt vmcnt(11)
	ds_write_b128 v82, v[128:131] offset:49152
	s_waitcnt vmcnt(10)
	ds_write_b128 v82, v[132:135] offset:53248
	s_waitcnt vmcnt(9)
	ds_write_b128 v82, v[144:147] offset:57344
	s_waitcnt vmcnt(8)
	ds_write_b128 v82, v[148:151] offset:61440
	s_waitcnt lgkmcnt(0)
	s_barrier
	ds_read_b128 v[100:103], v83 offset:32768
	ds_read_b128 v[104:107], v84 offset:49152
	ds_read_b128 v[120:123], v83 offset:36864
	ds_read_b128 v[124:127], v84 offset:53248
	v_mfma_f32_32x32x16_f16 v[2:17], v[136:139], v[140:143], v[2:17]
	s_waitcnt lgkmcnt(2)
	v_mfma_f32_32x32x16_f16 v[50:65], v[100:103], v[104:107], v[50:65]
	s_waitcnt lgkmcnt(0)
	v_mfma_f32_32x32x16_f16 v[18:33], v[100:103], v[124:127], v[18:33]
	v_mfma_f32_32x32x16_f16 v[34:49], v[120:123], v[104:107], v[34:49]
	v_mfma_f32_32x32x16_f16 v[2:17], v[120:123], v[124:127], v[2:17]
	ds_read_b128 v[100:103], v85 offset:32768
	ds_read_b128 v[104:107], v86 offset:49152
	ds_read_b128 v[120:123], v85 offset:36864
	ds_read_b128 v[124:127], v86 offset:53248
	s_waitcnt lgkmcnt(2)
	v_mfma_f32_32x32x16_f16 v[50:65], v[100:103], v[104:107], v[50:65]
	s_waitcnt lgkmcnt(0)
	v_mfma_f32_32x32x16_f16 v[18:33], v[100:103], v[124:127], v[18:33]
	v_mfma_f32_32x32x16_f16 v[34:49], v[120:123], v[104:107], v[34:49]
	v_mfma_f32_32x32x16_f16 v[2:17], v[120:123], v[124:127], v[2:17]
	ds_read_b128 v[100:103], v90 offset:32768
	ds_read_b128 v[104:107], v94 offset:49152
	ds_read_b128 v[120:123], v90 offset:36864
	ds_read_b128 v[124:127], v94 offset:53248
	s_waitcnt lgkmcnt(2)
	v_mfma_f32_32x32x16_f16 v[50:65], v[100:103], v[104:107], v[50:65]
	s_waitcnt lgkmcnt(0)
	v_mfma_f32_32x32x16_f16 v[18:33], v[100:103], v[124:127], v[18:33]
	v_mfma_f32_32x32x16_f16 v[34:49], v[120:123], v[104:107], v[34:49]
	v_mfma_f32_32x32x16_f16 v[2:17], v[120:123], v[124:127], v[2:17]
	ds_read_b128 v[100:103], v98 offset:32768
	ds_read_b128 v[104:107], v110 offset:49152
	ds_read_b128 v[120:123], v98 offset:36864
	ds_read_b128 v[124:127], v110 offset:53248
	s_waitcnt lgkmcnt(2)
	v_mfma_f32_32x32x16_f16 v[50:65], v[100:103], v[104:107], v[50:65]
	s_waitcnt lgkmcnt(0)
	v_mfma_f32_32x32x16_f16 v[18:33], v[100:103], v[124:127], v[18:33]
	v_mfma_f32_32x32x16_f16 v[34:49], v[120:123], v[104:107], v[34:49]
	global_load_dwordx4 v[100:103], v[66:67], off offset:640
	global_load_dwordx4 v[104:107], v[68:69], off offset:640
	global_load_dwordx4 v[128:131], v[70:71], off offset:640
	global_load_dwordx4 v[132:135], v[72:73], off offset:640
	global_load_dwordx4 v[136:139], v[74:75], off offset:640
	global_load_dwordx4 v[140:143], v[76:77], off offset:640
	global_load_dwordx4 v[144:147], v[78:79], off offset:640
	global_load_dwordx4 v[148:151], v[80:81], off offset:640
	s_waitcnt vmcnt(15)
	ds_write_b128 v82, v[112:115]
	s_waitcnt vmcnt(14)
	ds_write_b128 v82, v[116:119] offset:4096
	s_waitcnt vmcnt(13)
	ds_write_b128 v82, v[152:155] offset:8192
	s_waitcnt vmcnt(12)
	ds_write_b128 v82, v[156:159] offset:12288
	s_waitcnt vmcnt(11)
	ds_write_b128 v82, v[160:163] offset:16384
	s_waitcnt vmcnt(10)
	ds_write_b128 v82, v[164:167] offset:20480
	s_waitcnt vmcnt(9)
	ds_write_b128 v82, v[168:171] offset:24576
	s_waitcnt vmcnt(8)
	ds_write_b128 v82, v[172:175] offset:28672
	s_waitcnt lgkmcnt(0)
	s_barrier
	v_mfma_f32_32x32x16_f16 v[2:17], v[120:123], v[124:127], v[2:17]
	ds_read_b128 v[112:115], v83
	ds_read_b128 v[116:119], v84 offset:16384
	ds_read_b128 v[120:123], v83 offset:4096
	ds_read_b128 v[124:127], v84 offset:20480
	s_waitcnt lgkmcnt(2)
	v_mfma_f32_32x32x16_f16 v[50:65], v[112:115], v[116:119], v[50:65]
	s_waitcnt lgkmcnt(0)
	v_mfma_f32_32x32x16_f16 v[18:33], v[112:115], v[124:127], v[18:33]
	v_mfma_f32_32x32x16_f16 v[34:49], v[120:123], v[116:119], v[34:49]
	v_mfma_f32_32x32x16_f16 v[2:17], v[120:123], v[124:127], v[2:17]
	ds_read_b128 v[112:115], v85
	ds_read_b128 v[116:119], v86 offset:16384
	ds_read_b128 v[120:123], v85 offset:4096
	ds_read_b128 v[124:127], v86 offset:20480
	s_waitcnt lgkmcnt(2)
	v_mfma_f32_32x32x16_f16 v[50:65], v[112:115], v[116:119], v[50:65]
	s_waitcnt lgkmcnt(0)
	v_mfma_f32_32x32x16_f16 v[18:33], v[112:115], v[124:127], v[18:33]
	v_mfma_f32_32x32x16_f16 v[34:49], v[120:123], v[116:119], v[34:49]
	v_mfma_f32_32x32x16_f16 v[2:17], v[120:123], v[124:127], v[2:17]
	ds_read_b128 v[112:115], v90
	ds_read_b128 v[116:119], v94 offset:16384
	ds_read_b128 v[120:123], v90 offset:4096
	ds_read_b128 v[124:127], v94 offset:20480
	s_waitcnt lgkmcnt(2)
	v_mfma_f32_32x32x16_f16 v[50:65], v[112:115], v[116:119], v[50:65]
	s_waitcnt lgkmcnt(0)
	v_mfma_f32_32x32x16_f16 v[18:33], v[112:115], v[124:127], v[18:33]
	v_mfma_f32_32x32x16_f16 v[34:49], v[120:123], v[116:119], v[34:49]
	v_mfma_f32_32x32x16_f16 v[2:17], v[120:123], v[124:127], v[2:17]
	ds_read_b128 v[112:115], v98
	ds_read_b128 v[116:119], v110 offset:16384
	ds_read_b128 v[120:123], v98 offset:4096
	ds_read_b128 v[124:127], v110 offset:20480
	global_load_dwordx4 v[152:155], v[66:67], off offset:768
	global_load_dwordx4 v[156:159], v[68:69], off offset:768
	global_load_dwordx4 v[160:163], v[70:71], off offset:768
	global_load_dwordx4 v[164:167], v[72:73], off offset:768
	global_load_dwordx4 v[168:171], v[74:75], off offset:768
	global_load_dwordx4 v[172:175], v[76:77], off offset:768
	global_load_dwordx4 v[176:179], v[78:79], off offset:768
	global_load_dwordx4 v[206:209], v[80:81], off offset:768
	s_waitcnt vmcnt(15)
	ds_write_b128 v82, v[100:103] offset:32768
	s_waitcnt vmcnt(14)
	ds_write_b128 v82, v[104:107] offset:36864
	s_waitcnt vmcnt(13)
	ds_write_b128 v82, v[128:131] offset:40960
	s_waitcnt vmcnt(12)
	ds_write_b128 v82, v[132:135] offset:45056
	s_waitcnt vmcnt(11)
	ds_write_b128 v82, v[136:139] offset:49152
	s_waitcnt vmcnt(10)
	ds_write_b128 v82, v[140:143] offset:53248
	s_waitcnt vmcnt(9)
	ds_write_b128 v82, v[144:147] offset:57344
	s_waitcnt vmcnt(8)
	ds_write_b128 v82, v[148:151] offset:61440
	s_waitcnt lgkmcnt(0)
	s_barrier
	v_mfma_f32_32x32x16_f16 v[50:65], v[112:115], v[116:119], v[50:65]
	v_mfma_f32_32x32x16_f16 v[18:33], v[112:115], v[124:127], v[18:33]
	v_mfma_f32_32x32x16_f16 v[34:49], v[120:123], v[116:119], v[34:49]
	ds_read_b128 v[100:103], v83 offset:32768
	ds_read_b128 v[104:107], v84 offset:49152
	ds_read_b128 v[112:115], v83 offset:36864
	ds_read_b128 v[116:119], v84 offset:53248
	global_load_dwordx4 v[222:225], v[66:67], off offset:896
	global_load_dwordx4 v[226:229], v[68:69], off offset:896
	ds_read_b128 v[66:69], v85 offset:32768
	global_load_dwordx4 v[230:233], v[70:71], off offset:896
	global_load_dwordx4 v[234:237], v[72:73], off offset:896
	ds_read_b128 v[202:205], v86 offset:49152
	global_load_dwordx4 v[242:245], v[74:75], off offset:896
	s_nop 0
	global_load_dwordx4 v[74:77], v[76:77], off offset:896
	ds_read_b128 v[186:189], v85 offset:36864
	ds_read_b128 v[190:193], v86 offset:53248
	global_load_dwordx4 v[246:249], v[78:79], off offset:896
	s_nop 0
	global_load_dwordx4 v[78:81], v[80:81], off offset:896
	s_waitcnt lgkmcnt(6)
	v_mfma_f32_32x32x16_f16 v[50:65], v[100:103], v[104:107], v[50:65]
	v_mfma_f32_32x32x16_f16 v[2:17], v[120:123], v[124:127], v[2:17]
	s_waitcnt lgkmcnt(4)
	v_mfma_f32_32x32x16_f16 v[18:33], v[100:103], v[116:119], v[18:33]
	s_waitcnt lgkmcnt(2)
	v_mfma_f32_32x32x16_f16 v[50:65], v[66:69], v[202:205], v[50:65]
	v_mfma_f32_32x32x16_f16 v[34:49], v[112:115], v[104:107], v[34:49]
	v_mfma_f32_32x32x16_f16 v[2:17], v[112:115], v[116:119], v[2:17]
	ds_read_b128 v[198:201], v90 offset:32768
	ds_read_b128 v[114:117], v90 offset:36864
	ds_read_b128 v[182:185], v94 offset:49152
	ds_read_b128 v[122:125], v94 offset:53248
	ds_read_b128 v[130:133], v98 offset:32768
	ds_read_b128 v[102:105], v98 offset:36864
	ds_read_b128 v[194:197], v110 offset:49152
	ds_read_b128 v[106:109], v110 offset:53248
	s_waitcnt vmcnt(15)
	ds_write_b128 v82, v[152:155]
	s_waitcnt vmcnt(14)
	ds_write_b128 v82, v[156:159] offset:4096
	s_waitcnt vmcnt(13)
	ds_write_b128 v82, v[160:163] offset:8192
	s_waitcnt vmcnt(12)
	ds_write_b128 v82, v[164:167] offset:12288
	s_waitcnt lgkmcnt(12)
	v_mfma_f32_32x32x16_f16 v[18:33], v[66:69], v[190:193], v[18:33]
	s_waitcnt vmcnt(11)
	ds_write_b128 v82, v[168:171] offset:16384
	s_waitcnt vmcnt(10)
	ds_write_b128 v82, v[172:175] offset:20480
	s_waitcnt vmcnt(9)
	ds_write_b128 v82, v[176:179] offset:24576
	s_waitcnt vmcnt(8)
	ds_write_b128 v82, v[206:209] offset:28672
	s_waitcnt lgkmcnt(0)
	s_barrier
	ds_read_b128 v[162:165], v83
	ds_read_b128 v[206:209], v84 offset:16384
	ds_read_b128 v[150:153], v83 offset:4096
	ds_read_b128 v[154:157], v84 offset:20480
	ds_read_b128 v[158:161], v85
	ds_read_b128 v[134:137], v85 offset:4096
	ds_read_b128 v[210:213], v86 offset:16384
	ds_read_b128 v[142:145], v86 offset:20480
	ds_read_b128 v[146:149], v90
	ds_read_b128 v[118:121], v90 offset:4096
	ds_read_b128 v[214:217], v94 offset:16384
	ds_read_b128 v[126:129], v94 offset:20480
	ds_read_b128 v[138:141], v98
	ds_read_b128 v[66:69], v98 offset:4096
	ds_read_b128 v[218:221], v110 offset:16384
	ds_read_b128 v[70:73], v110 offset:20480
	v_mfma_f32_32x32x16_f16 v[50:65], v[198:201], v[182:185], v[50:65]
	s_waitcnt vmcnt(7)
	ds_write_b128 v82, v[222:225] offset:32768
	s_waitcnt vmcnt(6)
	ds_write_b128 v82, v[226:229] offset:36864
	s_waitcnt vmcnt(5)
	ds_write_b128 v82, v[230:233] offset:40960
	s_waitcnt vmcnt(4)
	ds_write_b128 v82, v[234:237] offset:45056
	s_waitcnt vmcnt(3)
	ds_write_b128 v82, v[242:245] offset:49152
	s_waitcnt vmcnt(2)
	ds_write_b128 v82, v[74:77] offset:53248
	s_waitcnt vmcnt(1)
	ds_write_b128 v82, v[246:249] offset:57344
	s_waitcnt vmcnt(0)
	ds_write_b128 v82, v[78:81] offset:61440
	s_waitcnt lgkmcnt(0)
	s_barrier
	ds_read_b128 v[166:169], v83 offset:32768
	ds_read_b128 v[222:225], v84 offset:49152
	ds_read_b128 v[74:77], v83 offset:36864
	ds_read_b128 v[78:81], v84 offset:53248
	ds_read_b128 v[170:173], v85 offset:32768
	ds_read_b128 v[82:85], v85 offset:36864
	ds_read_b128 v[226:229], v86 offset:49152
	ds_read_b128 v[86:89], v86 offset:53248
	ds_read_b128 v[174:177], v90 offset:32768
	ds_read_b128 v[90:93], v90 offset:36864
	ds_read_b128 v[230:233], v94 offset:49152
	ds_read_b128 v[94:97], v94 offset:53248
	ds_read_b128 v[178:181], v98 offset:32768
	ds_read_b128 v[98:101], v98 offset:36864
	ds_read_b128 v[234:237], v110 offset:49152
	ds_read_b128 v[110:113], v110 offset:53248
	s_waitcnt lgkmcnt(0)
	s_barrier
	v_mfma_f32_32x32x16_f16 v[50:65], v[130:133], v[194:197], v[50:65]
	v_lshlrev_b64 v[242:243], 11, v[240:241]
	v_lshl_add_u64 v[242:243], v[0:1], 0, v[242:243]
	v_or_b32_e32 v238, 59, v240
	v_mfma_f32_32x32x16_f16 v[50:65], v[162:165], v[206:209], v[50:65]
	v_mfma_f32_32x32x16_f16 v[50:65], v[158:161], v[210:213], v[50:65]
	v_mfma_f32_32x32x16_f16 v[50:65], v[146:149], v[214:217], v[50:65]
	v_mfma_f32_32x32x16_f16 v[50:65], v[138:141], v[218:221], v[50:65]
	v_mfma_f32_32x32x16_f16 v[34:49], v[186:189], v[202:205], v[34:49]
	v_mov_b32_e32 v203, v239
	v_mfma_f32_32x32x16_f16 v[50:65], v[166:169], v[222:225], v[50:65]
	v_mfma_f32_32x32x16_f16 v[34:49], v[114:117], v[182:185], v[34:49]
	v_mov_b32_e32 v185, v239
	v_mfma_f32_32x32x16_f16 v[50:65], v[170:173], v[226:229], v[50:65]
	v_mfma_f32_32x32x16_f16 v[34:49], v[102:105], v[194:197], v[34:49]
	v_mov_b32_e32 v195, v239
	v_mov_b32_e32 v197, v239
	v_mfma_f32_32x32x16_f16 v[50:65], v[174:177], v[230:233], v[50:65]
	v_mfma_f32_32x32x16_f16 v[34:49], v[150:153], v[206:209], v[34:49]
	v_mfma_f32_32x32x16_f16 v[2:17], v[186:189], v[190:193], v[2:17]
	v_mov_b32_e32 v189, v239
	v_mov_b32_e32 v191, v239
	v_mov_b32_e32 v193, v239
	v_mfma_f32_32x32x16_f16 v[50:65], v[178:181], v[234:237], v[50:65]
	v_mfma_f32_32x32x16_f16 v[34:49], v[134:137], v[210:213], v[34:49]
	s_waitcnt vmcnt(1)
	s_nop 9
	v_add_f32_e32 v50, v251, v50
	global_store_dword v[242:243], v50, off sc1
	v_or_b32_e32 v50, 1, v240
	v_add_f32_e32 v202, v251, v51
	v_mov_b32_e32 v51, v239
	v_lshlrev_b64 v[50:51], 11, v[50:51]
	v_lshl_add_u64 v[50:51], v[0:1], 0, v[50:51]
	v_mfma_f32_32x32x16_f16 v[18:33], v[198:201], v[122:125], v[18:33]
	global_store_dword v[50:51], v202, off sc1
	v_or_b32_e32 v202, 2, v240
	v_lshlrev_b64 v[186:187], 11, v[202:203]
	v_add_f32_e32 v52, v251, v52
	v_lshl_add_u64 v[186:187], v[0:1], 0, v[186:187]
	global_store_dword v[186:187], v52, off sc1
	v_or_b32_e32 v52, 3, v240
	v_mfma_f32_32x32x16_f16 v[2:17], v[114:117], v[122:125], v[2:17]
	v_add_f32_e32 v188, v251, v53
	v_mov_b32_e32 v53, v239
	v_lshlrev_b64 v[52:53], 11, v[52:53]
	v_lshl_add_u64 v[52:53], v[0:1], 0, v[52:53]
	global_store_dword v[52:53], v188, off sc1
	v_or_b32_e32 v188, 8, v240
	v_lshlrev_b64 v[188:189], 11, v[188:189]
	v_mfma_f32_32x32x16_f16 v[34:49], v[118:121], v[214:217], v[34:49]
	v_add_f32_e32 v54, v251, v54
	v_lshl_add_u64 v[182:183], v[0:1], 0, v[188:189]
	global_store_dword v[182:183], v54, off sc1
	v_or_b32_e32 v54, 9, v240
	v_add_f32_e32 v184, v251, v55
	v_mov_b32_e32 v55, v239
	v_lshlrev_b64 v[54:55], 11, v[54:55]
	v_mfma_f32_32x32x16_f16 v[18:33], v[130:133], v[106:109], v[18:33]
	v_lshl_add_u64 v[54:55], v[0:1], 0, v[54:55]
	global_store_dword v[54:55], v184, off sc1
	v_or_b32_e32 v184, 10, v240
	v_lshlrev_b64 v[184:185], 11, v[184:185]
	v_add_f32_e32 v56, v251, v56
	v_lshl_add_u64 v[184:185], v[0:1], 0, v[184:185]
	global_store_dword v[184:185], v56, off sc1
	v_mfma_f32_32x32x16_f16 v[2:17], v[102:105], v[106:109], v[2:17]
	v_or_b32_e32 v56, 11, v240
	v_add_f32_e32 v188, v251, v57
	v_mov_b32_e32 v57, v239
	v_lshlrev_b64 v[56:57], 11, v[56:57]
	v_lshl_add_u64 v[56:57], v[0:1], 0, v[56:57]
	global_store_dword v[56:57], v188, off sc1
	v_or_b32_e32 v188, 16, v240
	v_mfma_f32_32x32x16_f16 v[34:49], v[66:69], v[218:221], v[34:49]
	v_mov_b32_e32 v189, v239
	v_lshlrev_b64 v[188:189], 11, v[188:189]
	v_add_f32_e32 v58, v251, v58
	v_lshl_add_u64 v[188:189], v[0:1], 0, v[188:189]
	global_store_dword v[188:189], v58, off sc1
	v_or_b32_e32 v58, 17, v240
	v_add_f32_e32 v190, v251, v59
	v_mfma_f32_32x32x16_f16 v[18:33], v[162:165], v[154:157], v[18:33]
	v_mov_b32_e32 v59, v239
	v_lshlrev_b64 v[58:59], 11, v[58:59]
	v_lshl_add_u64 v[58:59], v[0:1], 0, v[58:59]
	global_store_dword v[58:59], v190, off sc1
	v_or_b32_e32 v190, 18, v240
	v_lshlrev_b64 v[190:191], 11, v[190:191]
	v_add_f32_e32 v60, v251, v60
	v_mfma_f32_32x32x16_f16 v[2:17], v[150:153], v[154:157], v[2:17]
	v_lshl_add_u64 v[190:191], v[0:1], 0, v[190:191]
	global_store_dword v[190:191], v60, off sc1
	v_or_b32_e32 v60, 19, v240
	v_add_f32_e32 v192, v251, v61
	v_mov_b32_e32 v61, v239
	v_lshlrev_b64 v[60:61], 11, v[60:61]
	v_lshl_add_u64 v[60:61], v[0:1], 0, v[60:61]
	v_mfma_f32_32x32x16_f16 v[34:49], v[74:77], v[222:225], v[34:49]
	global_store_dword v[60:61], v192, off sc1
	v_or_b32_e32 v192, 24, v240
	v_lshlrev_b64 v[192:193], 11, v[192:193]
	v_add_f32_e32 v62, v251, v62
	v_lshl_add_u64 v[192:193], v[0:1], 0, v[192:193]
	global_store_dword v[192:193], v62, off sc1
	v_or_b32_e32 v62, 25, v240
	v_mfma_f32_32x32x16_f16 v[18:33], v[158:161], v[142:145], v[18:33]
	v_add_f32_e32 v194, v251, v63
	v_mov_b32_e32 v63, v239
	v_lshlrev_b64 v[62:63], 11, v[62:63]
	v_lshl_add_u64 v[62:63], v[0:1], 0, v[62:63]
	global_store_dword v[62:63], v194, off sc1
	v_or_b32_e32 v194, 26, v240
	v_lshlrev_b64 v[194:195], 11, v[194:195]
	v_mfma_f32_32x32x16_f16 v[2:17], v[134:137], v[142:145], v[2:17]
	v_add_f32_e32 v64, v251, v64
	v_lshl_add_u64 v[194:195], v[0:1], 0, v[194:195]
	global_store_dword v[194:195], v64, off sc1
	v_or_b32_e32 v64, 27, v240
	v_add_f32_e32 v196, v251, v65
	v_mov_b32_e32 v65, v239
	v_lshlrev_b64 v[64:65], 11, v[64:65]
	v_mfma_f32_32x32x16_f16 v[34:49], v[82:85], v[226:229], v[34:49]
	v_lshl_add_u64 v[64:65], v[0:1], 0, v[64:65]
	global_store_dword v[64:65], v196, off sc1
	v_or_b32_e32 v196, 32, v240
	v_lshlrev_b64 v[114:115], 11, v[196:197]
	v_lshl_add_u64 v[114:115], v[0:1], 0, v[114:115]
	v_mov_b32_e32 v117, v239
	v_mov_b32_e32 v105, v239
	v_mfma_f32_32x32x16_f16 v[18:33], v[146:149], v[126:129], v[18:33]
	v_mov_b32_e32 v107, v239
	v_mov_b32_e32 v109, v239
	v_mfma_f32_32x32x16_f16 v[2:17], v[118:121], v[126:129], v[2:17]
	v_mov_b32_e32 v119, v239
	v_mov_b32_e32 v121, v239
	v_mfma_f32_32x32x16_f16 v[34:49], v[90:93], v[230:233], v[34:49]
	v_mfma_f32_32x32x16_f16 v[18:33], v[138:141], v[70:73], v[18:33]
	v_mfma_f32_32x32x16_f16 v[2:17], v[66:69], v[70:73], v[2:17]
	v_mfma_f32_32x32x16_f16 v[34:49], v[98:101], v[234:237], v[34:49]
	v_mfma_f32_32x32x16_f16 v[18:33], v[166:169], v[78:81], v[18:33]
	s_nop 10
	v_add_f32_e32 v34, v251, v34
	global_store_dword v[114:115], v34, off sc1
	v_or_b32_e32 v34, 33, v240
	v_add_f32_e32 v116, v251, v35
	v_mov_b32_e32 v35, v239
	v_lshlrev_b64 v[34:35], 11, v[34:35]
	v_lshl_add_u64 v[34:35], v[0:1], 0, v[34:35]
	v_mfma_f32_32x32x16_f16 v[2:17], v[74:77], v[78:81], v[2:17]
	global_store_dword v[34:35], v116, off sc1
	v_or_b32_e32 v116, 34, v240
	v_lshlrev_b64 v[116:117], 11, v[116:117]
	v_add_f32_e32 v36, v251, v36
	v_lshl_add_u64 v[102:103], v[0:1], 0, v[116:117]
	global_store_dword v[102:103], v36, off sc1
	v_or_b32_e32 v36, 35, v240
	v_mfma_f32_32x32x16_f16 v[18:33], v[170:173], v[86:89], v[18:33]
	v_add_f32_e32 v104, v251, v37
	v_mov_b32_e32 v37, v239
	v_lshlrev_b64 v[36:37], 11, v[36:37]
	v_lshl_add_u64 v[36:37], v[0:1], 0, v[36:37]
	global_store_dword v[36:37], v104, off sc1
	v_or_b32_e32 v104, 40, v240
	v_lshlrev_b64 v[104:105], 11, v[104:105]
	v_mfma_f32_32x32x16_f16 v[2:17], v[82:85], v[86:89], v[2:17]
	v_add_f32_e32 v38, v251, v38
	v_lshl_add_u64 v[104:105], v[0:1], 0, v[104:105]
	global_store_dword v[104:105], v38, off sc1
	v_or_b32_e32 v38, 41, v240
	v_add_f32_e32 v106, v251, v39
	v_mov_b32_e32 v39, v239
	v_lshlrev_b64 v[38:39], 11, v[38:39]
	v_mfma_f32_32x32x16_f16 v[18:33], v[174:177], v[94:97], v[18:33]
	v_lshl_add_u64 v[38:39], v[0:1], 0, v[38:39]
	global_store_dword v[38:39], v106, off sc1
	v_or_b32_e32 v106, 42, v240
	v_lshlrev_b64 v[106:107], 11, v[106:107]
	v_add_f32_e32 v40, v251, v40
	v_lshl_add_u64 v[106:107], v[0:1], 0, v[106:107]
	global_store_dword v[106:107], v40, off sc1
	v_mfma_f32_32x32x16_f16 v[2:17], v[90:93], v[94:97], v[2:17]
	v_or_b32_e32 v40, 43, v240
	v_add_f32_e32 v108, v251, v41
	v_mov_b32_e32 v41, v239
	v_lshlrev_b64 v[40:41], 11, v[40:41]
	v_lshl_add_u64 v[40:41], v[0:1], 0, v[40:41]
	global_store_dword v[40:41], v108, off sc1
	v_or_b32_e32 v108, 48, v240
	v_mfma_f32_32x32x16_f16 v[18:33], v[178:181], v[110:113], v[18:33]
	v_lshlrev_b64 v[108:109], 11, v[108:109]
	v_add_f32_e32 v42, v251, v42
	v_lshl_add_u64 v[108:109], v[0:1], 0, v[108:109]
	global_store_dword v[108:109], v42, off sc1
	v_or_b32_e32 v42, 49, v240
	v_add_f32_e32 v116, v251, v43
	v_mov_b32_e32 v43, v239
	v_mfma_f32_32x32x16_f16 v[2:17], v[98:101], v[110:113], v[2:17]
	v_lshlrev_b64 v[42:43], 11, v[42:43]
	v_lshl_add_u64 v[42:43], v[0:1], 0, v[42:43]
	global_store_dword v[42:43], v116, off sc1
	v_or_b32_e32 v116, 50, v240
	v_mov_b32_e32 v117, v239
	v_lshlrev_b64 v[116:117], 11, v[116:117]
	s_waitcnt vmcnt(26)
	v_add_f32_e32 v18, v252, v18
	s_nop 3
	v_add_f32_e32 v2, v252, v2
	v_add_f32_e32 v44, v251, v44
	v_lshl_add_u64 v[116:117], v[0:1], 0, v[116:117]
	global_store_dword v[242:243], v18, off offset:128 sc1
	v_add_f32_e32 v18, v252, v19
	global_store_dword v[114:115], v2, off offset:128 sc1
	v_add_f32_e32 v2, v252, v3
	global_store_dword v[116:117], v44, off sc1
	v_or_b32_e32 v44, 51, v240
	v_add_f32_e32 v118, v251, v45
	v_mov_b32_e32 v45, v239
	global_store_dword v[50:51], v18, off offset:128 sc1
	v_add_f32_e32 v18, v252, v20
	global_store_dword v[34:35], v2, off offset:128 sc1
	v_add_f32_e32 v2, v252, v4
	v_lshlrev_b64 v[44:45], 11, v[44:45]
	global_store_dword v[186:187], v18, off offset:128 sc1
	v_add_f32_e32 v18, v252, v21
	global_store_dword v[102:103], v2, off offset:128 sc1
	v_add_f32_e32 v2, v252, v5
	v_lshl_add_u64 v[44:45], v[0:1], 0, v[44:45]
	global_store_dword v[52:53], v18, off offset:128 sc1
	v_add_f32_e32 v18, v252, v22
	global_store_dword v[36:37], v2, off offset:128 sc1
	v_add_f32_e32 v2, v252, v6
	global_store_dword v[44:45], v118, off sc1
	v_or_b32_e32 v118, 56, v240
	global_store_dword v[182:183], v18, off offset:128 sc1
	v_add_f32_e32 v18, v252, v23
	global_store_dword v[104:105], v2, off offset:128 sc1
	v_add_f32_e32 v2, v252, v7
	v_lshlrev_b64 v[118:119], 11, v[118:119]
	global_store_dword v[54:55], v18, off offset:128 sc1
	v_add_f32_e32 v18, v252, v24
	global_store_dword v[38:39], v2, off offset:128 sc1
	v_add_f32_e32 v2, v252, v8
	v_add_f32_e32 v46, v251, v46
	v_lshl_add_u64 v[118:119], v[0:1], 0, v[118:119]
	global_store_dword v[184:185], v18, off offset:128 sc1
	v_add_f32_e32 v18, v252, v25
	global_store_dword v[106:107], v2, off offset:128 sc1
	v_add_f32_e32 v2, v252, v9
	global_store_dword v[118:119], v46, off sc1
	v_or_b32_e32 v46, 57, v240
	v_add_f32_e32 v120, v251, v47
	v_mov_b32_e32 v47, v239
	global_store_dword v[56:57], v18, off offset:128 sc1
	v_add_f32_e32 v18, v252, v26
	global_store_dword v[40:41], v2, off offset:128 sc1
	v_add_f32_e32 v2, v252, v10
	v_lshlrev_b64 v[46:47], 11, v[46:47]
	global_store_dword v[188:189], v18, off offset:128 sc1
	v_add_f32_e32 v18, v252, v27
	global_store_dword v[108:109], v2, off offset:128 sc1
	v_add_f32_e32 v2, v252, v11
	v_lshl_add_u64 v[46:47], v[0:1], 0, v[46:47]
	global_store_dword v[58:59], v18, off offset:128 sc1
	v_add_f32_e32 v18, v252, v28
	global_store_dword v[42:43], v2, off offset:128 sc1
	v_add_f32_e32 v2, v252, v12
	global_store_dword v[46:47], v120, off sc1
	v_or_b32_e32 v120, 58, v240
	global_store_dword v[190:191], v18, off offset:128 sc1
	v_add_f32_e32 v18, v252, v29
	global_store_dword v[116:117], v2, off offset:128 sc1
	v_add_f32_e32 v2, v252, v13
	v_lshlrev_b64 v[120:121], 11, v[120:121]
	global_store_dword v[60:61], v18, off offset:128 sc1
	v_add_f32_e32 v18, v252, v30
	global_store_dword v[44:45], v2, off offset:128 sc1
	v_add_f32_e32 v2, v252, v14
	v_add_f32_e32 v48, v251, v48
	v_lshl_add_u64 v[120:121], v[0:1], 0, v[120:121]
	global_store_dword v[192:193], v18, off offset:128 sc1
	v_add_f32_e32 v18, v252, v31
	global_store_dword v[118:119], v2, off offset:128 sc1
	v_add_f32_e32 v2, v252, v15
	global_store_dword v[120:121], v48, off sc1
	v_add_f32_e32 v122, v251, v49
	v_lshlrev_b64 v[48:49], 11, v[238:239]
	global_store_dword v[62:63], v18, off offset:128 sc1
	v_add_f32_e32 v18, v252, v32
	global_store_dword v[46:47], v2, off offset:128 sc1
	v_add_f32_e32 v2, v252, v16
	v_lshl_add_u64 v[0:1], v[0:1], 0, v[48:49]
	global_store_dword v[194:195], v18, off offset:128 sc1
	v_add_f32_e32 v18, v252, v33
	global_store_dword v[120:121], v2, off offset:128 sc1
	v_add_f32_e32 v2, v252, v17
	global_store_dword v[0:1], v122, off sc1
	global_store_dword v[64:65], v18, off offset:128 sc1
	global_store_dword v[0:1], v2, off offset:128 sc1
	s_endpgm
	.p2align	8
